# attention: the next-batch counter atomic is left in flight (no vmcnt(0) drain of the K/V prefetch queue at batch ends), its value read three items later
# speedup vs baseline: 1.0048x; 1.0048x over previous
.LBB0_530:
	s_or_b64 exec, exec, s[0:1]
	s_and_b32 s30, s10, 3
	s_cmp_lt_u32 s11, 4
	s_cselect_b64 s[54:55], -1, 0
	s_and_b64 s[0:1], s[54:55], exec
	s_movk_i32 s0, 0x1f00
	s_cselect_b32 s31, 0x2000, s0
	v_readfirstlane_b32 s58, v0
	v_lshl_or_b32 v182, s30, 7, v161
	s_cmp_ge_i32 s58, s31
	s_cbranch_scc1 .LBB0_565
	v_mov_b32_e32 v136, 0
	s_and_saveexec_b64 s[0:1], s[36:37]
	s_cbranch_execz .LBB0_535
	s_mov_b64 s[8:9], exec
	v_mbcnt_lo_u32_b32 v0, s8, 0
	v_mbcnt_hi_u32_b32 v0, s9, v0
	v_cmp_eq_u32_e32 vcc, 0, v0
	s_and_saveexec_b64 s[6:7], vcc
	s_cbranch_execz .LBB0_534
	s_bcnt1_i32_b64 s8, s[8:9]
	s_lshl_b32 s8, s8, 2
	v_mov_b32_e32 v136, s8
	global_atomic_add v136, v137, v136, s[52:53] sc0
.LBB0_534:
	s_or_b64 exec, exec, s[6:7]
.LBB0_535:
	s_or_b64 exec, exec, s[0:1]
	s_and_b64 s[0:1], s[54:55], exec
	s_movk_i32 s0, 0x1fff
	s_cselect_b32 s59, 0x3fff, s0
	s_sub_i32 s56, s59, s58
	s_mov_b32 s57, s5
	s_lshl_b64 s[0:1], s[56:57], 9
	v_lshl_add_u64 v[0:1], v[144:145], 0, s[0:1]
	global_load_ushort v2, v[0:1], off
	global_load_ushort v5, v[0:1], off offset:128
	global_load_ushort v6, v[0:1], off offset:256
	global_load_ushort v7, v[0:1], off offset:384
	s_lshl_b32 s6, s30, 9
	s_mul_i32 s0, s56, 0x1100
	v_add_u32_e32 v183, s6, v163
	s_waitcnt vmcnt(0)
	v_mov_b32_e32 v4, 0
	v_mov_b32_e32 v3, 0
	ds_write_b16 v162, v2 offset:18432
	ds_write_b16 v162, v5 offset:18560
	ds_write_b16 v162, v6 offset:18688
	ds_write_b16 v162, v7 offset:18816
	v_mov_b32_e32 v1, 0
	v_mov_b32_e32 v2, 0
	v_add_u32_e32 v0, s0, v183
	v_lshl_add_u32 v16, v0, 1, v164
	v_mov_b32_e32 v0, 0
	s_and_saveexec_b64 s[0:1], s[38:39]
	s_cbranch_execz .LBB0_537
	global_load_dwordx4 v[0:3], v16, s[44:45]

.LBB0_555:
	s_or_b64 exec, exec, s[6:7]
	s_nop 4
	ds_read_b128 v[80:83], v168
	s_ashr_i32 s57, s56, 31
	s_lshl_b64 s[6:7], s[56:57], 12
	v_lshl_add_u64 v[84:85], v[156:157], 0, s[6:7]
	s_andn2_b64 vcc, exec, s[0:1]
	s_waitcnt lgkmcnt(0)
	global_store_dwordx4 v[84:85], v[80:83], off
	s_cbranch_vccnz .LBB0_563
	s_andn2_b64 vcc, exec, s[8:9]
	s_cbranch_vccnz .LBB0_562
	v_mov_b32_e32 v136, 0
	s_and_saveexec_b64 s[6:7], s[36:37]
	s_cbranch_execz .LBB0_561
	s_mov_b64 s[10:11], exec
	v_mbcnt_lo_u32_b32 v80, s10, 0
	v_mbcnt_hi_u32_b32 v80, s11, v80
	v_cmp_eq_u32_e32 vcc, 0, v80
	s_and_saveexec_b64 s[8:9], vcc
	s_cbranch_execz .LBB0_560
	s_bcnt1_i32_b64 s10, s[10:11]
	s_lshl_b32 s10, s10, 2
	v_mov_b32_e32 v136, s10
	global_atomic_add v136, v137, v136, s[52:53] sc0
.LBB0_560:
	s_or_b64 exec, exec, s[8:9]
.LBB0_561:
	s_or_b64 exec, exec, s[6:7]
	s_mov_b32 s64, 0
	s_mov_b32 s58, s29
